# quad-local chain (mixer final pass..router) replaces 5 grid barriers; attention LDS read rings; residual GEMM epilogues restructured; spin caps as in original barrier
# baseline (speedup 1.0000x reference)
.Lqs7_spin:
	global_load_dword v2, v0, s[8:9] sc1
	s_waitcnt vmcnt(0)
	v_readfirstlane_b32 s0, v2
	s_nop 3
	s_cmp_ge_u32 s0, 4
	s_cbranch_scc1 .Lqs7_done
	s_sleep 1
	s_add_u32 s1, s1, 1
	s_cmp_lt_u32 s1, 0x400000
	s_cbranch_scc1 .Lqs7_spin
